# Hyena unit set-up: filter reversal moved after the whole load burst (no wait between the unit's ten loads)
# speedup vs baseline: 1.0065x; 1.0065x over previous
.LBB0_928:
	v_mbcnt_lo_u32_b32 v176, -1, 0
	v_mbcnt_hi_u32_b32 v176, -1, v176
	s_getreg_b32 s6, hwreg(HW_REG_HW_ID, 0, 6)
	s_lshl_b32 s6, s6, 2
	s_and_b32 s6, s6, 0xfc
	s_or_b32 s6, s6, 0x27100
	v_mov_b32_e32 v0, s6
	s_lshl_b32 s6, s17, 5
	s_and_b32 s6, s6, 0xe0
	s_ashr_i32 s7, s17, 3
	s_or_b32 s8, s6, s7
	s_mov_b32 s6, 35
	ds_read_b32 v0, v0
	s_ashr_i32 s7, s6, 31
	s_lshl_b64 s[6:7], s[6:7], 3
	s_add_u32 s6, s0, s6
	s_addc_u32 s7, s1, s7
	s_load_dwordx2 s[10:11], s[6:7], 0x0
	s_add_i32 s6, s8, s16
	s_ashr_i32 s7, s6, 31
	s_waitcnt lgkmcnt(0)
	v_readfirstlane_b32 s9, v0
	s_lshl_b64 s[12:13], s[6:7], 14
	s_waitcnt vmcnt(0)
	v_lshl_or_b32 v0, s9, 6, v176
	s_add_u32 s9, s10, s12
	s_addc_u32 s10, s11, s13
	v_lshlrev_b32_e32 v2, 3, v0
	s_add_u32 s9, s9, 0x1003ff0
	v_ashrrev_i32_e32 v3, 31, v2
	s_addc_u32 s10, s10, 0
	v_lshlrev_b64 v[38:39], 1, v[2:3]
	v_mov_b32_e32 v3, s10
	v_sub_co_u32_e32 v4, vcc, s9, v38
	v_add_u32_e32 v2, 0x1000, v2
	s_nop 0
	v_subb_co_u32_e32 v5, vcc, v3, v39, vcc
	v_ashrrev_i32_e32 v3, 31, v2
	v_lshlrev_b64 v[2:3], 1, v[2:3]
	v_mov_b32_e32 v7, s10
	v_sub_co_u32_e32 v6, vcc, s9, v2
	s_mov_b32 s10, 35
	s_nop 0
	v_subb_co_u32_e32 v7, vcc, v7, v3, vcc
	s_barrier
	global_load_dwordx4 v[2:5], v[4:5], off
	s_nop 0
	global_load_dwordx4 v[6:9], v[6:7], off
	s_ashr_i32 s11, s10, 31
	s_lshl_b64 s[10:11], s[10:11], 3
	s_add_u32 s10, s0, s10
	s_addc_u32 s11, s1, s11
	s_load_dwordx2 s[12:13], s[10:11], 0x0
	s_ashr_i32 s9, s8, 31
	s_lshl_b64 s[10:11], s[8:9], 13
	s_mov_b32 s9, 0x34600000
	v_lshl_add_u32 v46, v0, 4, 0
	s_waitcnt lgkmcnt(0)
	s_add_u32 s12, s12, s10
	s_addc_u32 s13, s13, s11
	v_lshl_add_u64 v[10:11], s[12:13], 0, v[38:39]
	v_add_co_u32_e32 v10, vcc, s83, v10
	s_mov_b32 s12, 35
	s_nop 0
	v_addc_co_u32_e32 v11, vcc, 0, v11, vcc
	global_load_dwordx4 v[10:13], v[10:11], off
	s_ashr_i32 s13, s12, 31
	s_lshl_b64 s[12:13], s[12:13], 3
	s_add_u32 s12, s0, s12
	s_addc_u32 s13, s1, s13
	s_load_dwordx2 s[12:13], s[12:13], 0x0
	v_add_u32_e32 v47, 0x10100, v46
	s_waitcnt lgkmcnt(0)
	s_add_u32 s12, s12, s10
	s_addc_u32 s13, s13, s11
	v_lshl_add_u64 v[14:15], s[12:13], 0, v[38:39]
	v_add_co_u32_e32 v14, vcc, s9, v14
	s_mov_b32 s12, 35
	s_nop 0
	v_addc_co_u32_e32 v15, vcc, 0, v15, vcc
	global_load_dwordx4 v[14:17], v[14:15], off
	s_ashr_i32 s13, s12, 31
	s_lshl_b64 s[12:13], s[12:13], 3
	s_add_u32 s12, s0, s12
	s_addc_u32 s13, s1, s13
	s_load_dwordx2 s[12:13], s[12:13], 0x0
	s_mov_b32 s9, 0x34800000
	s_waitcnt lgkmcnt(0)
	s_add_u32 s12, s12, s10
	s_addc_u32 s13, s13, s11
	v_lshl_add_u64 v[18:19], s[12:13], 0, v[38:39]
	v_add_co_u32_e32 v18, vcc, s9, v18
	s_mov_b32 s12, 35
	s_nop 0
	v_addc_co_u32_e32 v19, vcc, 0, v19, vcc
	global_load_dwordx4 v[18:21], v[18:19], off
	s_ashr_i32 s13, s12, 31
	s_lshl_b64 s[12:13], s[12:13], 3
	s_add_u32 s12, s0, s12
	s_addc_u32 s13, s1, s13
	s_load_dwordx2 s[12:13], s[12:13], 0x0
	s_mov_b32 s9, 0x34a00000
	s_waitcnt lgkmcnt(0)
	s_add_u32 s12, s12, s10
	s_addc_u32 s13, s13, s11
	v_lshl_add_u64 v[22:23], s[12:13], 0, v[38:39]
	v_add_co_u32_e32 v22, vcc, s9, v22
	s_mov_b32 s12, 35
	s_nop 0
	v_addc_co_u32_e32 v23, vcc, 0, v23, vcc
	global_load_dwordx4 v[22:25], v[22:23], off
	s_ashr_i32 s13, s12, 31
	s_lshl_b64 s[12:13], s[12:13], 3
	s_add_u32 s12, s0, s12
	s_addc_u32 s13, s1, s13
	s_load_dwordx2 s[12:13], s[12:13], 0x0
	s_mov_b32 s9, 0x34c00000
	s_waitcnt lgkmcnt(0)
	s_add_u32 s12, s12, s10
	s_addc_u32 s13, s13, s11
	v_lshl_add_u64 v[26:27], s[12:13], 0, v[38:39]
	v_add_co_u32_e32 v26, vcc, s9, v26
	s_mov_b32 s12, 35
	s_nop 0
	v_addc_co_u32_e32 v27, vcc, 0, v27, vcc
	global_load_dwordx4 v[26:29], v[26:27], off
	s_ashr_i32 s13, s12, 31
	s_lshl_b64 s[12:13], s[12:13], 3
	s_add_u32 s12, s0, s12
	s_addc_u32 s13, s1, s13
	s_load_dwordx2 s[12:13], s[12:13], 0x0
	s_mov_b32 s9, 0x34e00000
	s_waitcnt lgkmcnt(0)
	s_add_u32 s12, s12, s10
	s_addc_u32 s13, s13, s11
	v_lshl_add_u64 v[30:31], s[12:13], 0, v[38:39]
	v_add_co_u32_e32 v30, vcc, s9, v30
	s_mov_b32 s12, 35
	s_nop 0
	v_addc_co_u32_e32 v31, vcc, 0, v31, vcc
	global_load_dwordx4 v[30:33], v[30:31], off
	s_ashr_i32 s13, s12, 31
	s_lshl_b64 s[12:13], s[12:13], 3
	s_add_u32 s12, s0, s12
	s_addc_u32 s13, s1, s13
	s_load_dwordx2 s[12:13], s[12:13], 0x0
	s_mov_b32 s9, 0x35000000
	s_waitcnt lgkmcnt(0)
	s_add_u32 s12, s12, s10
	s_addc_u32 s13, s13, s11
	v_lshl_add_u64 v[34:35], s[12:13], 0, v[38:39]
	v_add_co_u32_e32 v34, vcc, s9, v34
	s_mov_b32 s12, 35
	s_nop 0
	v_addc_co_u32_e32 v35, vcc, 0, v35, vcc
	global_load_dwordx4 v[34:37], v[34:35], off
	s_ashr_i32 s13, s12, 31
	s_lshl_b64 s[12:13], s[12:13], 3
	s_add_u32 s12, s0, s12
	s_addc_u32 s13, s1, s13
	s_load_dwordx2 s[12:13], s[12:13], 0x0
	s_mov_b32 s9, 0x35200000
	s_waitcnt lgkmcnt(0)
	s_add_u32 s10, s12, s10
	s_addc_u32 s11, s13, s11
	v_lshl_add_u64 v[38:39], s[10:11], 0, v[38:39]
	v_add_co_u32_e32 v38, vcc, s9, v38
	v_readfirstlane_b32 s9, v0
	s_nop 0
	v_addc_co_u32_e32 v39, vcc, 0, v39, vcc
	global_load_dwordx4 v[38:41], v[38:39], off
	v_cmp_gt_i32_e32 vcc, 32, v0
	s_waitcnt vmcnt(9)
	v_alignbit_b32 v42, v5, v5, 16
	v_alignbit_b32 v43, v4, v4, 16
	v_alignbit_b32 v44, v3, v3, 16
	v_alignbit_b32 v45, v2, v2, 16
	s_waitcnt vmcnt(8)
	v_alignbit_b32 v2, v9, v9, 16
	v_alignbit_b32 v3, v8, v8, 16
	v_alignbit_b32 v4, v7, v7, 16
	v_alignbit_b32 v5, v6, v6, 16
	ds_write_b128 v46, v[42:45]
	ds_write_b128 v46, v[2:5] offset:8192
	s_waitcnt vmcnt(7)
	ds_write_b128 v47, v[10:13]
	s_waitcnt vmcnt(6)
	ds_write_b128 v47, v[14:17] offset:8224
	s_waitcnt vmcnt(5)
	ds_write_b128 v47, v[18:21] offset:16448
	s_waitcnt vmcnt(4)
	ds_write_b128 v47, v[22:25] offset:24672
	s_waitcnt vmcnt(3)
	ds_write_b128 v47, v[26:29] offset:32896
	s_waitcnt vmcnt(2)
	ds_write_b128 v47, v[30:33] offset:41120
	s_waitcnt vmcnt(1)
	ds_write_b128 v47, v[34:37] offset:49344
	s_waitcnt vmcnt(0)
	ds_write_b128 v47, v[38:41] offset:57568
	s_and_saveexec_b64 s[10:11], vcc
	v_lshl_add_u32 v2, v0, 2, 0
	v_add_u32_e32 v2, 0x20200, v2
	ds_write_b32 v2, v1
	s_or_b64 exec, exec, s[10:11]
	s_movk_i32 s10, 0x3000
	v_cmp_gt_i32_e32 vcc, s10, v0
	s_waitcnt lgkmcnt(0)
	s_barrier
	s_and_saveexec_b64 s[10:11], vcc
	s_cbranch_execz .LBB0_935
	s_mov_b64 s[12:13], 0
	v_mov_b32_e32 v2, v0
	s_branch .LBB0_933
